# s_setprio 1/0 around the P.V MFMA groups of both attention tile loops (on top of the DMA-rebalanced K-loops version)
# baseline (speedup 1.0000x reference)
.Latt0_sk3:
	v_exp_f32_e32 v91, v91
	v_add_f32_e32 v202, v87, v202
	v_exp_f32_e32 v92, v92
	v_add_f32_e32 v202, v88, v202
	v_exp_f32_e32 v93, v93
	v_add_f32_e32 v202, v89, v202
	v_exp_f32_e32 v94, v94
	v_add_f32_e32 v202, v90, v202
	ds_read_b128 v[224:227], v192 offset:49152
	ds_read_b128 v[220:223], v191 offset:49152
	ds_read_b128 v[228:231], v191 offset:57344
	ds_read_b128 v[232:235], v193 offset:49152
	v_exp_f32_e32 v95, v95
	v_add_f32_e32 v202, v91, v202
	v_add_f32_e32 v202, v92, v202
	v_add_f32_e32 v202, v93, v202
	v_add_f32_e32 v202, v94, v202
	v_add_f32_e32 v202, v95, v202
	v_mov_b32_e32 v203, v202
	s_nop 1
	s_waitcnt lgkmcnt(0)
	v_mfma_f32_32x32x64_f8f6f4 v[112:127], v[220:227], v[144:151], v[112:127]
	v_permlane32_swap_b32_e32 v202, v203
	v_cvt_pk_bf16_f32 v204, v64, v65
	v_cvt_pk_bf16_f32 v205, v66, v67
	v_cvt_pk_bf16_f32 v206, v68, v69
	v_cvt_pk_bf16_f32 v207, v70, v71
	v_cvt_pk_bf16_f32 v208, v72, v73
	v_cvt_pk_bf16_f32 v209, v74, v75
	v_cvt_pk_bf16_f32 v210, v76, v77
	v_cvt_pk_bf16_f32 v211, v78, v79
	v_cvt_pk_bf16_f32 v212, v80, v81
	v_cvt_pk_bf16_f32 v213, v82, v83
	v_mfma_f32_32x32x64_f8f6f4 v[96:111], v[228:235], v[144:151], v[96:111]
	v_cvt_pk_bf16_f32 v214, v84, v85
	v_cvt_pk_bf16_f32 v215, v86, v87
	v_cvt_pk_bf16_f32 v216, v88, v89
	v_cvt_pk_bf16_f32 v217, v90, v91
	v_cvt_pk_bf16_f32 v218, v92, v93
	v_cvt_pk_bf16_f32 v219, v94, v95
	s_nop 0
	v_permlane32_swap_b32_e32 v204, v206
	v_permlane32_swap_b32_e32 v205, v207
	v_permlane32_swap_b32_e32 v208, v210
	v_permlane32_swap_b32_e32 v209, v211
	v_permlane32_swap_b32_e32 v212, v214
	v_permlane32_swap_b32_e32 v213, v215
	v_permlane32_swap_b32_e32 v216, v218
	v_permlane32_swap_b32_e32 v217, v219
	ds_read_b64_tr_b16 v[220:221], v190 offset:0
	ds_read_b64_tr_b16 v[222:223], v190 offset:0x800
	ds_read_b64_tr_b16 v[224:225], v190 offset:0x1000
	ds_read_b64_tr_b16 v[226:227], v190 offset:0x1800
	ds_read_b64_tr_b16 v[228:229], v190 offset:0x2000
	ds_read_b64_tr_b16 v[230:231], v190 offset:0x2800
	ds_read_b64_tr_b16 v[232:233], v190 offset:0x3000
	ds_read_b64_tr_b16 v[234:235], v190 offset:0x3800
	v_max_f32_e32 v200, v113, v113
	v_max_f32_e32 v240, v112, v112
	v_max_f32_e32 v200, v240, v200
	v_max3_f32 v200, v200, v114, v115
	v_max3_f32 v200, v200, v116, v117
	v_max3_f32 v200, v200, v118, v119
	v_max3_f32 v200, v200, v120, v121
	v_max3_f32 v200, v200, v122, v123
	s_waitcnt lgkmcnt(0)
	s_nop 0
	s_setprio 1
	v_mfma_f32_32x32x16_bf16 v[0:15], v[204:207], v[220:223], v[0:15]
	v_max3_f32 v200, v200, v124, v125
	v_max3_f32 v200, v200, v126, v127
	v_max3_f32 v200, v200, v96, v97
	v_max3_f32 v200, v200, v98, v99
	v_max3_f32 v200, v200, v100, v101
	ds_read_b64_tr_b16 v[220:221], v190 offset:0x200
	ds_read_b64_tr_b16 v[222:223], v190 offset:0xa00
	v_mfma_f32_32x32x16_bf16 v[0:15], v[208:211], v[224:227], v[0:15]
	v_max3_f32 v200, v200, v102, v103
	v_max3_f32 v200, v200, v104, v105
	v_max3_f32 v200, v200, v106, v107
	v_max3_f32 v200, v200, v108, v109
	v_max3_f32 v200, v200, v110, v111
	ds_read_b64_tr_b16 v[224:225], v190 offset:0x1200
	ds_read_b64_tr_b16 v[226:227], v190 offset:0x1a00
	v_mfma_f32_32x32x16_bf16 v[0:15], v[212:215], v[228:231], v[0:15]
	v_mov_b32_e32 v240, v200
	s_nop 1
	v_permlane32_swap_b32_e32 v200, v240
	ds_read_b64_tr_b16 v[228:229], v190 offset:0x2200
	ds_read_b64_tr_b16 v[230:231], v190 offset:0x2a00
	ds_read_b64_tr_b16 v[236:237], v190 offset:0x3200
	ds_read_b64_tr_b16 v[238:239], v190 offset:0x3a00
	v_max_f32_e32 v240, v240, v240
	v_max_f32_e32 v200, v200, v200
	v_max_f32_e32 v200, v200, v240
	v_sub_f32_e32 v240, v200, v195
	v_cmp_ge_f32_e32 vcc, s93, v240
	v_max_f32_e32 v240, v195, v195
	v_max_f32_e32 v240, v240, v200
	v_sub_f32_e32 v200, v195, v240
	s_waitcnt lgkmcnt(0)
	v_mfma_f32_32x32x16_bf16 v[0:15], v[216:219], v[232:235], v[0:15]
	v_mul_f32_e32 v200, 0x3dd53b94, v200
	v_exp_f32_e32 v200, v200
	s_cmp_eq_u64 vcc, exec
	s_cselect_b64 s[6:7], -1, 0
	v_mfma_f32_32x32x16_bf16 v[48:63], v[204:207], v[220:223], v[48:63]
	v_cndmask_b32_e64 v200, v200, 1.0, s[6:7]
	v_cmp_gt_f32_e32 vcc, 1.0, v200
	v_cndmask_b32_e64 v195, v240, v195, s[6:7]
	v_mul_f32_e32 v240, 0xbdd53b94, v195
	v_mov_b32_e32 v241, v240
	ds_read_b64_tr_b16 v[220:221], v190 offset:0x400
	ds_read_b64_tr_b16 v[222:223], v190 offset:0xc00
	v_mfma_f32_32x32x16_bf16 v[48:63], v[208:211], v[224:227], v[48:63]
	v_fmamk_f32 v112, v112, 0x3dd53b94, v240
	v_fmamk_f32 v113, v113, 0x3dd53b94, v240
	v_fmamk_f32 v114, v114, 0x3dd53b94, v240
	v_fmamk_f32 v115, v115, 0x3dd53b94, v240
	v_fmamk_f32 v116, v116, 0x3dd53b94, v240
	ds_read_b64_tr_b16 v[224:225], v190 offset:0x1400
	ds_read_b64_tr_b16 v[226:227], v190 offset:0x1c00
	v_mfma_f32_32x32x16_bf16 v[48:63], v[212:215], v[228:231], v[48:63]
	v_fmamk_f32 v117, v117, 0x3dd53b94, v240
	v_fmamk_f32 v118, v118, 0x3dd53b94, v240
	v_fmamk_f32 v119, v119, 0x3dd53b94, v240
	v_fmamk_f32 v120, v120, 0x3dd53b94, v240
	v_fmamk_f32 v121, v121, 0x3dd53b94, v240
	ds_read_b64_tr_b16 v[228:229], v190 offset:0x2400
	ds_read_b64_tr_b16 v[230:231], v190 offset:0x2c00
	ds_read_b64_tr_b16 v[232:233], v190 offset:0x3400
	ds_read_b64_tr_b16 v[234:235], v190 offset:0x3c00
	v_fmamk_f32 v122, v122, 0x3dd53b94, v240
	v_fmamk_f32 v123, v123, 0x3dd53b94, v240
	v_fmamk_f32 v124, v124, 0x3dd53b94, v240
	v_fmamk_f32 v125, v125, 0x3dd53b94, v240
	v_fmamk_f32 v126, v126, 0x3dd53b94, v240
	v_fmac_f32_e32 v241, 0x3dd53b94, v127
	v_exp_f32_e32 v112, v112
	s_waitcnt lgkmcnt(0)
	v_mfma_f32_32x32x16_bf16 v[48:63], v[216:219], v[236:239], v[48:63]
	v_exp_f32_e32 v113, v113
	v_exp_f32_e32 v114, v114
	v_mfma_f32_32x32x16_bf16 v[32:47], v[204:207], v[220:223], v[32:47]
	v_exp_f32_e32 v115, v115
	v_exp_f32_e32 v116, v116
	ds_read_b64_tr_b16 v[220:221], v190 offset:0x600
	ds_read_b64_tr_b16 v[222:223], v190 offset:0xe00
	v_mfma_f32_32x32x16_bf16 v[32:47], v[208:211], v[224:227], v[32:47]
	v_exp_f32_e32 v117, v117
	v_exp_f32_e32 v118, v118
	ds_read_b64_tr_b16 v[224:225], v190 offset:0x1600
	ds_read_b64_tr_b16 v[226:227], v190 offset:0x1e00
	v_mfma_f32_32x32x16_bf16 v[32:47], v[212:215], v[228:231], v[32:47]
	v_exp_f32_e32 v119, v119
	v_exp_f32_e32 v120, v120
	ds_read_b64_tr_b16 v[228:229], v190 offset:0x2600
	ds_read_b64_tr_b16 v[230:231], v190 offset:0x2e00
	ds_read_b64_tr_b16 v[236:237], v190 offset:0x3600
	ds_read_b64_tr_b16 v[238:239], v190 offset:0x3e00
	v_exp_f32_e32 v121, v121
	v_exp_f32_e32 v122, v122
	v_exp_f32_e32 v123, v123
	v_exp_f32_e32 v124, v124
	s_waitcnt lgkmcnt(0)
	v_mfma_f32_32x32x16_bf16 v[32:47], v[216:219], v[232:235], v[32:47]
	v_exp_f32_e32 v125, v125
	v_exp_f32_e32 v126, v126
	v_mfma_f32_32x32x16_bf16 v[16:31], v[204:207], v[220:223], v[16:31]
	v_exp_f32_e32 v127, v241
	v_pk_fma_f32 v[110:111], v[110:111], s[54:55], v[240:241] op_sel_hi:[1,0,0]
	v_mfma_f32_32x32x16_bf16 v[16:31], v[208:211], v[224:227], v[16:31]
	v_pk_fma_f32 v[108:109], v[108:109], s[54:55], v[240:241] op_sel_hi:[1,0,0]
	v_pk_fma_f32 v[106:107], v[106:107], s[54:55], v[240:241] op_sel_hi:[1,0,0]
	v_mfma_f32_32x32x16_bf16 v[16:31], v[212:215], v[228:231], v[16:31]
	v_pk_fma_f32 v[104:105], v[104:105], s[54:55], v[240:241] op_sel_hi:[1,0,0]
	v_pk_fma_f32 v[102:103], v[102:103], s[54:55], v[240:241] op_sel_hi:[1,0,0]
	v_mfma_f32_32x32x16_bf16 v[16:31], v[216:219], v[236:239], v[16:31]
	s_setprio 0
	v_pk_fma_f32 v[100:101], v[100:101], s[54:55], v[240:241] op_sel_hi:[1,0,0]
	v_pk_fma_f32 v[98:99], v[98:99], s[54:55], v[240:241] op_sel_hi:[1,0,0]
	v_pk_fma_f32 v[96:97], v[96:97], s[54:55], v[240:241] op_sel_hi:[1,0,0]
	s_cbranch_vccz .Latt0_nrA
	s_nop 7
	s_nop 7
	s_and_saveexec_b64 s[38:39], s[4:5]
	ds_write_b32 v197, v200 offset:128
	s_or_b64 exec, exec, s[38:39]
	s_waitcnt lgkmcnt(0)
	v_add_u32_e32 v205, s77, v196
	ds_read_b128 v[206:209], v205 offset:224
	ds_read_b128 v[210:213], v205 offset:192
	ds_read_b128 v[214:217], v205 offset:160
	ds_read_b128 v[218:221], v205 offset:128
	s_waitcnt lgkmcnt(0)
	v_pk_mul_f32 v[12:13], v[12:13], v[206:207]
	v_pk_mul_f32 v[8:9], v[8:9], v[210:211]
	v_pk_mul_f32 v[4:5], v[4:5], v[214:215]
	v_pk_mul_f32 v[14:15], v[14:15], v[208:209]
	v_pk_mul_f32 v[10:11], v[10:11], v[212:213]
	v_pk_mul_f32 v[6:7], v[6:7], v[216:217]
	v_pk_mul_f32 v[2:3], v[2:3], v[220:221]
	v_pk_mul_f32 v[0:1], v[0:1], v[218:219]
	v_pk_mul_f32 v[60:61], v[60:61], v[206:207]
	v_pk_mul_f32 v[56:57], v[56:57], v[210:211]
	v_pk_mul_f32 v[52:53], v[52:53], v[214:215]
	v_pk_mul_f32 v[62:63], v[62:63], v[208:209]
	v_pk_mul_f32 v[58:59], v[58:59], v[212:213]
	v_pk_mul_f32 v[54:55], v[54:55], v[216:217]
	v_pk_mul_f32 v[50:51], v[50:51], v[220:221]
	v_pk_mul_f32 v[48:49], v[48:49], v[218:219]
	v_pk_mul_f32 v[44:45], v[44:45], v[206:207]
	v_pk_mul_f32 v[40:41], v[40:41], v[210:211]
	v_pk_mul_f32 v[36:37], v[36:37], v[214:215]
	v_pk_mul_f32 v[46:47], v[46:47], v[208:209]
	v_pk_mul_f32 v[42:43], v[42:43], v[212:213]
	v_pk_mul_f32 v[38:39], v[38:39], v[216:217]
	v_pk_mul_f32 v[34:35], v[34:35], v[220:221]
	v_pk_mul_f32 v[32:33], v[32:33], v[218:219]
	v_pk_mul_f32 v[28:29], v[28:29], v[206:207]
	v_pk_mul_f32 v[24:25], v[24:25], v[210:211]
	v_pk_mul_f32 v[20:21], v[20:21], v[214:215]
	v_pk_mul_f32 v[30:31], v[30:31], v[208:209]
	v_pk_mul_f32 v[26:27], v[26:27], v[212:213]
	v_pk_mul_f32 v[22:23], v[22:23], v[216:217]
	v_pk_mul_f32 v[18:19], v[18:19], v[220:221]
	v_pk_mul_f32 v[16:17], v[16:17], v[218:219]
.Latt0_nrA:
.LBB0_511:
	s_add_i32 s6, s19, -1
	s_min_u32 s36, s6, s42
	s_mul_i32 s6, s36, 0x30000
	s_add_u32 s6, s64, s6
	s_addc_u32 s7, s65, 0
	s_add_i32 s43, s19, -2
	s_waitcnt vmcnt(0)
	v_lshl_add_u64 v[204:205], s[6:7], 0, v[152:153]
	s_cmp_lt_u32 s43, s33
	s_waitcnt lgkmcnt(0)
	s_waitcnt vmcnt(0) lgkmcnt(0)
	s_barrier
	s_mov_b64 s[46:47], s[6:7]
	s_cselect_b64 s[6:7], -1, 0
	s_min_u32 s38, s43, s42
	s_lshl_b32 s38, s38, 19
	s_add_u32 s38, s66, s38
	s_addc_u32 s39, s67, 0
	s_cmp_ge_u32 s43, s33
	s_cbranch_scc1 .Latt0_cold_mid
	ds_read_b128 v[68:71], v185 offset:32768
	ds_read_b128 v[64:67], v184 offset:32768
	ds_read_b128 v[80:83], v184 offset:40960
	ds_read_b128 v[84:87], v186 offset:32768
	ds_read_b128 v[226:229], v188 offset:32768
	ds_read_b128 v[222:225], v187 offset:32768
	v_add_f32_e32 v204, 0, v112
	v_add_f32_e32 v204, v113, v204
	v_add_f32_e32 v204, v114, v204
	v_add_f32_e32 v204, v115, v204
	v_add_f32_e32 v204, v116, v204
	v_add_f32_e32 v204, v117, v204
	v_add_f32_e32 v204, v118, v204
	v_add_f32_e32 v204, v119, v204
	v_add_f32_e32 v204, v120, v204
	v_add_f32_e32 v204, v121, v204
	s_waitcnt lgkmcnt(0)
	v_mfma_f32_32x32x64_f8f6f4 v[64:79], v[64:71], v[128:135], 0
	v_lshl_add_u64 v[246:247], s[46:47], 0, v[152:153]
	s_mov_b32 m0, s95
	s_nop 0
	global_load_lds_dwordx4 v[246:247], off
	v_add_f32_e32 v204, v122, v204
	v_add_f32_e32 v204, v123, v204
	v_exp_f32_e32 v96, v96
	v_add_f32_e32 v204, v124, v204
	v_exp_f32_e32 v97, v97
	v_add_f32_e32 v204, v125, v204
	v_exp_f32_e32 v98, v98
	v_add_f32_e32 v204, v126, v204
	v_mfma_f32_32x32x64_f8f6f4 v[80:95], v[80:87], v[128:135], 0
	v_lshl_add_u64 v[246:247], s[46:47], 0, v[154:155]
	s_mov_b32 m0, s18
	s_nop 0
	global_load_lds_dwordx4 v[246:247], off
	v_exp_f32_e32 v99, v99
	v_add_f32_e32 v204, v127, v204
	v_exp_f32_e32 v100, v100
	v_add_f32_e32 v204, v96, v204
	v_exp_f32_e32 v101, v101
	v_add_f32_e32 v204, v97, v204
	v_exp_f32_e32 v102, v102
	v_add_f32_e32 v204, v98, v204
	v_mfma_f32_32x32x64_f8f6f4 v[64:79], v[222:229], v[136:143], v[64:79]
	v_lshl_add_u64 v[246:247], s[38:39], 0, v[156:157]
	s_mov_b32 m0, s56
	s_nop 0
	global_load_lds_dwordx4 v[246:247], off
	v_exp_f32_e32 v103, v103
	v_add_f32_e32 v204, v99, v204
	v_exp_f32_e32 v104, v104
	v_add_f32_e32 v204, v100, v204
	v_exp_f32_e32 v105, v105
	v_add_f32_e32 v204, v101, v204
	v_exp_f32_e32 v106, v106
	v_add_f32_e32 v204, v102, v204
	ds_read_b128 v[222:225], v187 offset:40960
	ds_read_b128 v[226:229], v189 offset:32768
	v_exp_f32_e32 v107, v107
	v_add_f32_e32 v204, v103, v204
	v_exp_f32_e32 v108, v108
	v_add_f32_e32 v204, v104, v204
	v_exp_f32_e32 v109, v109
	v_add_f32_e32 v204, v105, v204
	s_waitcnt lgkmcnt(0)
	v_mfma_f32_32x32x64_f8f6f4 v[80:95], v[222:229], v[136:143], v[80:95]
	v_lshl_add_u64 v[246:247], s[38:39], 0, v[158:159]
	s_mov_b32 m0, s91
	s_nop 0
	global_load_lds_dwordx4 v[246:247], off
	v_exp_f32_e32 v110, v110
	v_add_f32_e32 v204, v106, v204
	v_exp_f32_e32 v111, v111
	v_add_f32_e32 v204, v107, v204
	v_add_f32_e32 v204, v108, v204
	v_add_f32_e32 v204, v109, v204
	v_add_f32_e32 v204, v110, v204
	v_add_f32_e32 v204, v111, v204
	v_mov_b32_e32 v205, v204
	ds_read_b128 v[226:229], v192 offset:32768
	ds_read_b128 v[222:225], v191 offset:32768
	s_nop 1
	v_permlane32_swap_b32_e32 v204, v205
	v_cvt_pk_bf16_f32 v206, v112, v113
	v_cvt_pk_bf16_f32 v207, v114, v115
	v_cvt_pk_bf16_f32 v208, v116, v117
	v_cvt_pk_bf16_f32 v209, v118, v119
	v_cvt_pk_bf16_f32 v210, v120, v121
	v_cvt_pk_bf16_f32 v211, v122, v123
	s_waitcnt lgkmcnt(0)
	v_mfma_f32_32x32x64_f8f6f4 v[64:79], v[222:229], v[144:151], v[64:79]
	v_cvt_pk_bf16_f32 v212, v124, v125
	v_cvt_pk_bf16_f32 v213, v126, v127
	v_cvt_pk_bf16_f32 v214, v96, v97
	v_cvt_pk_bf16_f32 v215, v98, v99
	v_cvt_pk_bf16_f32 v216, v100, v101
	v_cvt_pk_bf16_f32 v217, v102, v103
	v_cvt_pk_bf16_f32 v218, v104, v105
	v_cvt_pk_bf16_f32 v219, v106, v107
	v_cvt_pk_bf16_f32 v220, v108, v109
	v_cvt_pk_bf16_f32 v221, v110, v111
	s_nop 0
	ds_read_b128 v[222:225], v191 offset:40960
	ds_read_b128 v[226:229], v193 offset:32768
	v_permlane32_swap_b32_e32 v206, v208
	v_permlane32_swap_b32_e32 v207, v209
	v_permlane32_swap_b32_e32 v210, v212
	v_permlane32_swap_b32_e32 v211, v213
	v_permlane32_swap_b32_e32 v214, v216
	s_waitcnt lgkmcnt(0)
	v_mfma_f32_32x32x64_f8f6f4 v[80:95], v[222:229], v[144:151], v[80:95]
	v_permlane32_swap_b32_e32 v215, v217
	v_permlane32_swap_b32_e32 v218, v220
	v_permlane32_swap_b32_e32 v219, v221
	ds_read_b64_tr_b16 v[222:223], v199 offset:0
	ds_read_b64_tr_b16 v[224:225], v199 offset:0x800
	ds_read_b64_tr_b16 v[226:227], v199 offset:0x1000
	ds_read_b64_tr_b16 v[228:229], v199 offset:0x1800
	ds_read_b64_tr_b16 v[230:231], v199 offset:0x2000
	ds_read_b64_tr_b16 v[232:233], v199 offset:0x2800
	ds_read_b64_tr_b16 v[234:235], v199 offset:0x3000
	ds_read_b64_tr_b16 v[236:237], v199 offset:0x3800
	v_max_f32_e32 v242, v65, v65
	v_max_f32_e32 v243, v64, v64
	v_max_f32_e32 v242, v243, v242
	v_max3_f32 v242, v242, v66, v67
	v_max3_f32 v242, v242, v68, v69
	v_max3_f32 v242, v242, v70, v71
	v_max3_f32 v242, v242, v72, v73
	v_max3_f32 v242, v242, v74, v75
	s_waitcnt lgkmcnt(0)
	s_nop 0
	s_setprio 1
	v_mfma_f32_32x32x16_bf16 v[0:15], v[206:209], v[222:225], v[0:15]
	v_max3_f32 v242, v242, v76, v77
	v_max3_f32 v242, v242, v78, v79
	v_max3_f32 v242, v242, v80, v81
	v_max3_f32 v242, v242, v82, v83
	v_max3_f32 v242, v242, v84, v85
	ds_read_b64_tr_b16 v[222:223], v199 offset:0x200
	ds_read_b64_tr_b16 v[224:225], v199 offset:0xa00
	v_mfma_f32_32x32x16_bf16 v[0:15], v[210:213], v[226:229], v[0:15]
	v_max3_f32 v242, v242, v86, v87
	v_max3_f32 v242, v242, v88, v89
	v_max3_f32 v242, v242, v90, v91
	v_max3_f32 v242, v242, v92, v93
	v_max3_f32 v242, v242, v94, v95
	ds_read_b64_tr_b16 v[226:227], v199 offset:0x1200
	ds_read_b64_tr_b16 v[228:229], v199 offset:0x1a00
	v_mfma_f32_32x32x16_bf16 v[0:15], v[214:217], v[230:233], v[0:15]
	v_mov_b32_e32 v243, v242
	s_nop 1
	v_permlane32_swap_b32_e32 v242, v243
	ds_read_b64_tr_b16 v[230:231], v199 offset:0x2200
	ds_read_b64_tr_b16 v[232:233], v199 offset:0x2a00
	v_mfma_f32_32x32x16_bf16 v[0:15], v[218:221], v[234:237], v[0:15]
	v_max_f32_e32 v243, v243, v243
	v_max_f32_e32 v242, v242, v242
	v_max_f32_e32 v242, v242, v243
	v_sub_f32_e32 v243, v242, v195
	v_cmp_ge_f32_e32 vcc, s93, v243
	ds_read_b64_tr_b16 v[234:235], v199 offset:0x3200
	ds_read_b64_tr_b16 v[236:237], v199 offset:0x3a00
	v_max_f32_e32 v243, v195, v195
	v_max_f32_e32 v243, v243, v242
	v_sub_f32_e32 v242, v195, v243
	v_mul_f32_e32 v242, 0x3dd53b94, v242
	v_exp_f32_e32 v242, v242
	s_cmp_eq_u64 vcc, exec
	s_cselect_b64 s[6:7], -1, 0
	s_waitcnt lgkmcnt(0)
	v_mfma_f32_32x32x16_bf16 v[48:63], v[206:209], v[222:225], v[48:63]
	v_cndmask_b32_e64 v242, v242, 1.0, s[6:7]
	v_cmp_gt_f32_e32 vcc, 1.0, v242
	v_cndmask_b32_e64 v195, v243, v195, s[6:7]
	v_mul_f32_e32 v244, 0xbdd53b94, v195
	v_mov_b32_e32 v243, v244
	ds_read_b64_tr_b16 v[222:223], v199 offset:0x400
	ds_read_b64_tr_b16 v[224:225], v199 offset:0xc00
	v_mfma_f32_32x32x16_bf16 v[48:63], v[210:213], v[226:229], v[48:63]
	v_fmamk_f32 v64, v64, 0x3dd53b94, v244
	v_fmamk_f32 v65, v65, 0x3dd53b94, v244
	v_fmamk_f32 v66, v66, 0x3dd53b94, v244
	v_fmamk_f32 v67, v67, 0x3dd53b94, v244
	v_fmamk_f32 v68, v68, 0x3dd53b94, v244
	ds_read_b64_tr_b16 v[226:227], v199 offset:0x1400
	ds_read_b64_tr_b16 v[228:229], v199 offset:0x1c00
	v_mfma_f32_32x32x16_bf16 v[48:63], v[214:217], v[230:233], v[48:63]
	v_fmamk_f32 v69, v69, 0x3dd53b94, v244
	v_fmamk_f32 v70, v70, 0x3dd53b94, v244
	v_fmamk_f32 v71, v71, 0x3dd53b94, v244
	v_fmamk_f32 v72, v72, 0x3dd53b94, v244
	v_fmamk_f32 v73, v73, 0x3dd53b94, v244
	ds_read_b64_tr_b16 v[230:231], v199 offset:0x2400
	ds_read_b64_tr_b16 v[232:233], v199 offset:0x2c00
	v_mfma_f32_32x32x16_bf16 v[48:63], v[218:221], v[234:237], v[48:63]
	v_fmamk_f32 v74, v74, 0x3dd53b94, v244
	v_fmamk_f32 v75, v75, 0x3dd53b94, v244
	v_fmamk_f32 v76, v76, 0x3dd53b94, v244
	v_fmamk_f32 v77, v77, 0x3dd53b94, v244
	v_fmamk_f32 v78, v78, 0x3dd53b94, v244
	ds_read_b64_tr_b16 v[234:235], v199 offset:0x3400
	ds_read_b64_tr_b16 v[236:237], v199 offset:0x3c00
	v_fmac_f32_e32 v243, 0x3dd53b94, v79
	v_exp_f32_e32 v64, v64
	v_exp_f32_e32 v65, v65
	v_exp_f32_e32 v66, v66
	s_waitcnt lgkmcnt(0)
	v_mfma_f32_32x32x16_bf16 v[32:47], v[206:209], v[222:225], v[32:47]
	v_exp_f32_e32 v67, v67
	v_exp_f32_e32 v68, v68
	ds_read_b64_tr_b16 v[222:223], v199 offset:0x600
	ds_read_b64_tr_b16 v[224:225], v199 offset:0xe00
	v_mfma_f32_32x32x16_bf16 v[32:47], v[210:213], v[226:229], v[32:47]
	v_exp_f32_e32 v69, v69
	v_exp_f32_e32 v70, v70
	ds_read_b64_tr_b16 v[226:227], v199 offset:0x1600
	ds_read_b64_tr_b16 v[228:229], v199 offset:0x1e00
	v_mfma_f32_32x32x16_bf16 v[32:47], v[214:217], v[230:233], v[32:47]
	v_exp_f32_e32 v71, v71
	v_exp_f32_e32 v72, v72
	ds_read_b64_tr_b16 v[230:231], v199 offset:0x2600
	ds_read_b64_tr_b16 v[232:233], v199 offset:0x2e00
	v_mfma_f32_32x32x16_bf16 v[32:47], v[218:221], v[234:237], v[32:47]
	v_exp_f32_e32 v73, v73
	v_exp_f32_e32 v74, v74
	ds_read_b64_tr_b16 v[234:235], v199 offset:0x3600
	ds_read_b64_tr_b16 v[236:237], v199 offset:0x3e00
	v_exp_f32_e32 v75, v75
	v_exp_f32_e32 v76, v76
	v_exp_f32_e32 v77, v77
	v_exp_f32_e32 v78, v78
	s_waitcnt lgkmcnt(0)
	v_mfma_f32_32x32x16_bf16 v[16:31], v[206:209], v[222:225], v[16:31]
	v_exp_f32_e32 v79, v243
	v_pk_fma_f32 v[94:95], v[94:95], s[54:55], v[244:245] op_sel_hi:[1,0,0]
	v_mfma_f32_32x32x16_bf16 v[16:31], v[210:213], v[226:229], v[16:31]
	v_pk_fma_f32 v[92:93], v[92:93], s[54:55], v[244:245] op_sel_hi:[1,0,0]
	v_pk_fma_f32 v[90:91], v[90:91], s[54:55], v[244:245] op_sel_hi:[1,0,0]
	v_mfma_f32_32x32x16_bf16 v[16:31], v[214:217], v[230:233], v[16:31]
	v_pk_fma_f32 v[88:89], v[88:89], s[54:55], v[244:245] op_sel_hi:[1,0,0]
	v_pk_fma_f32 v[86:87], v[86:87], s[54:55], v[244:245] op_sel_hi:[1,0,0]
	v_mfma_f32_32x32x16_bf16 v[16:31], v[218:221], v[234:237], v[16:31]
	s_setprio 0
	v_pk_fma_f32 v[84:85], v[84:85], s[54:55], v[244:245] op_sel_hi:[1,0,0]
	v_pk_fma_f32 v[82:83], v[82:83], s[54:55], v[244:245] op_sel_hi:[1,0,0]
	v_pk_fma_f32 v[80:81], v[80:81], s[54:55], v[244:245] op_sel_hi:[1,0,0]
	v_mov_b32_e32 v206, v242
	s_cbranch_vccz .Latt0_nrB
	s_nop 7
	s_nop 7
	s_and_saveexec_b64 s[38:39], s[4:5]
	ds_write_b32 v197, v206 offset:128
	s_or_b64 exec, exec, s[38:39]
	s_waitcnt lgkmcnt(0)
	v_add_u32_e32 v220, s77, v196
	ds_read_b128 v[208:211], v220 offset:224
	ds_read_b128 v[212:215], v220 offset:192
	ds_read_b128 v[216:219], v220 offset:160
	ds_read_b128 v[220:223], v220 offset:128
	s_waitcnt lgkmcnt(0)
	v_pk_mul_f32 v[12:13], v[12:13], v[208:209]
	v_pk_mul_f32 v[8:9], v[8:9], v[212:213]
	v_pk_mul_f32 v[4:5], v[4:5], v[216:217]
	v_pk_mul_f32 v[14:15], v[14:15], v[210:211]
	v_pk_mul_f32 v[10:11], v[10:11], v[214:215]
	v_pk_mul_f32 v[6:7], v[6:7], v[218:219]
	v_pk_mul_f32 v[2:3], v[2:3], v[222:223]
	v_pk_mul_f32 v[0:1], v[0:1], v[220:221]
	v_pk_mul_f32 v[60:61], v[60:61], v[208:209]
	v_pk_mul_f32 v[56:57], v[56:57], v[212:213]
	v_pk_mul_f32 v[52:53], v[52:53], v[216:217]
	v_pk_mul_f32 v[62:63], v[62:63], v[210:211]
	v_pk_mul_f32 v[58:59], v[58:59], v[214:215]
	v_pk_mul_f32 v[54:55], v[54:55], v[218:219]
	v_pk_mul_f32 v[50:51], v[50:51], v[222:223]
	v_pk_mul_f32 v[48:49], v[48:49], v[220:221]
	v_pk_mul_f32 v[44:45], v[44:45], v[208:209]
	v_pk_mul_f32 v[40:41], v[40:41], v[212:213]
	v_pk_mul_f32 v[36:37], v[36:37], v[216:217]
	v_pk_mul_f32 v[46:47], v[46:47], v[210:211]
	v_pk_mul_f32 v[42:43], v[42:43], v[214:215]
	v_pk_mul_f32 v[38:39], v[38:39], v[218:219]
	v_pk_mul_f32 v[34:35], v[34:35], v[222:223]
	v_pk_mul_f32 v[32:33], v[32:33], v[220:221]
	v_pk_mul_f32 v[28:29], v[28:29], v[208:209]
	v_pk_mul_f32 v[24:25], v[24:25], v[212:213]
	v_pk_mul_f32 v[20:21], v[20:21], v[216:217]
	v_pk_mul_f32 v[30:31], v[30:31], v[210:211]
	v_pk_mul_f32 v[26:27], v[26:27], v[214:215]
	v_pk_mul_f32 v[22:23], v[22:23], v[218:219]
	v_pk_mul_f32 v[18:19], v[18:19], v[222:223]
	v_pk_mul_f32 v[16:17], v[16:17], v[220:221]

.LBB0_513:
	v_add_f32_e32 v204, 0, v112
	v_add_f32_e32 v204, v113, v204
	v_add_f32_e32 v204, v114, v204
	v_add_f32_e32 v204, v115, v204
	v_add_f32_e32 v204, v116, v204
	v_add_f32_e32 v204, v117, v204
	v_add_f32_e32 v204, v118, v204
	v_add_f32_e32 v204, v119, v204
	v_add_f32_e32 v204, v120, v204
	v_add_f32_e32 v204, v121, v204
	v_add_f32_e32 v204, v122, v204
	v_add_f32_e32 v204, v123, v204
	v_exp_f32_e32 v96, v96
	v_add_f32_e32 v204, v124, v204
	v_exp_f32_e32 v97, v97
	v_add_f32_e32 v204, v125, v204
	v_exp_f32_e32 v98, v98
	v_add_f32_e32 v204, v126, v204
	v_exp_f32_e32 v99, v99
	v_add_f32_e32 v204, v127, v204
	v_exp_f32_e32 v100, v100
	v_add_f32_e32 v204, v96, v204
	v_exp_f32_e32 v101, v101
	v_add_f32_e32 v204, v97, v204
	v_exp_f32_e32 v102, v102
	v_add_f32_e32 v204, v98, v204
	v_exp_f32_e32 v103, v103
	v_add_f32_e32 v204, v99, v204
	v_exp_f32_e32 v104, v104
	v_add_f32_e32 v204, v100, v204
	v_exp_f32_e32 v105, v105
	v_add_f32_e32 v204, v101, v204
	v_exp_f32_e32 v106, v106
	v_add_f32_e32 v204, v102, v204
	v_exp_f32_e32 v107, v107
	v_add_f32_e32 v204, v103, v204
	v_exp_f32_e32 v108, v108
	v_add_f32_e32 v204, v104, v204
	v_exp_f32_e32 v109, v109
	v_add_f32_e32 v204, v105, v204
	v_exp_f32_e32 v110, v110
	v_add_f32_e32 v204, v106, v204
	v_exp_f32_e32 v111, v111
	v_add_f32_e32 v204, v107, v204
	v_add_f32_e32 v204, v108, v204
	v_add_f32_e32 v204, v109, v204
	v_add_f32_e32 v204, v110, v204
	v_add_f32_e32 v204, v111, v204
	v_mov_b32_e32 v205, v204
	s_nop 1
	v_permlane32_swap_b32_e32 v204, v205
	v_cvt_pk_bf16_f32 v206, v112, v113
	v_cvt_pk_bf16_f32 v207, v114, v115
	v_cvt_pk_bf16_f32 v208, v116, v117
	v_cvt_pk_bf16_f32 v209, v118, v119
	v_cvt_pk_bf16_f32 v210, v120, v121
	v_cvt_pk_bf16_f32 v211, v122, v123
	v_cvt_pk_bf16_f32 v212, v124, v125
	v_cvt_pk_bf16_f32 v213, v126, v127
	v_cvt_pk_bf16_f32 v214, v96, v97
	v_cvt_pk_bf16_f32 v215, v98, v99
	v_cvt_pk_bf16_f32 v216, v100, v101
	v_cvt_pk_bf16_f32 v217, v102, v103
	v_cvt_pk_bf16_f32 v218, v104, v105
	v_cvt_pk_bf16_f32 v219, v106, v107
	v_cvt_pk_bf16_f32 v220, v108, v109
	v_cvt_pk_bf16_f32 v221, v110, v111
	s_nop 0
	v_permlane32_swap_b32_e32 v206, v208
	v_permlane32_swap_b32_e32 v207, v209
	v_permlane32_swap_b32_e32 v210, v212
	v_permlane32_swap_b32_e32 v211, v213
	v_permlane32_swap_b32_e32 v214, v216
	v_permlane32_swap_b32_e32 v215, v217
	v_permlane32_swap_b32_e32 v218, v220
	v_permlane32_swap_b32_e32 v219, v221
	ds_read_b64_tr_b16 v[222:223], v199 offset:0
	ds_read_b64_tr_b16 v[224:225], v199 offset:0x800
	ds_read_b64_tr_b16 v[226:227], v199 offset:0x1000
	ds_read_b64_tr_b16 v[228:229], v199 offset:0x1800
	ds_read_b64_tr_b16 v[230:231], v199 offset:0x2000
	ds_read_b64_tr_b16 v[232:233], v199 offset:0x2800
	ds_read_b64_tr_b16 v[234:235], v199 offset:0x3000
	ds_read_b64_tr_b16 v[236:237], v199 offset:0x3800
	s_waitcnt lgkmcnt(0)
	s_nop 0
	s_setprio 1
	v_mfma_f32_32x32x16_bf16 v[0:15], v[206:209], v[222:225], v[0:15]
	ds_read_b64_tr_b16 v[222:223], v199 offset:0x200
	ds_read_b64_tr_b16 v[224:225], v199 offset:0xa00
	v_mfma_f32_32x32x16_bf16 v[0:15], v[210:213], v[226:229], v[0:15]
	ds_read_b64_tr_b16 v[226:227], v199 offset:0x1200
	ds_read_b64_tr_b16 v[228:229], v199 offset:0x1a00
	v_mfma_f32_32x32x16_bf16 v[0:15], v[214:217], v[230:233], v[0:15]
	ds_read_b64_tr_b16 v[230:231], v199 offset:0x2200
	ds_read_b64_tr_b16 v[232:233], v199 offset:0x2a00
	v_mfma_f32_32x32x16_bf16 v[0:15], v[218:221], v[234:237], v[0:15]
	ds_read_b64_tr_b16 v[234:235], v199 offset:0x3200
	ds_read_b64_tr_b16 v[236:237], v199 offset:0x3a00
	s_waitcnt lgkmcnt(0)
	v_mfma_f32_32x32x16_bf16 v[48:63], v[206:209], v[222:225], v[48:63]
	ds_read_b64_tr_b16 v[222:223], v199 offset:0x400
	ds_read_b64_tr_b16 v[224:225], v199 offset:0xc00
	v_mfma_f32_32x32x16_bf16 v[48:63], v[210:213], v[226:229], v[48:63]
	ds_read_b64_tr_b16 v[226:227], v199 offset:0x1400
	ds_read_b64_tr_b16 v[228:229], v199 offset:0x1c00
	v_mfma_f32_32x32x16_bf16 v[48:63], v[214:217], v[230:233], v[48:63]
	ds_read_b64_tr_b16 v[230:231], v199 offset:0x2400
	ds_read_b64_tr_b16 v[232:233], v199 offset:0x2c00
	v_mfma_f32_32x32x16_bf16 v[48:63], v[218:221], v[234:237], v[48:63]
	ds_read_b64_tr_b16 v[234:235], v199 offset:0x3400
	ds_read_b64_tr_b16 v[236:237], v199 offset:0x3c00
	s_waitcnt lgkmcnt(0)
	v_mfma_f32_32x32x16_bf16 v[32:47], v[206:209], v[222:225], v[32:47]
	ds_read_b64_tr_b16 v[222:223], v199 offset:0x600
	ds_read_b64_tr_b16 v[224:225], v199 offset:0xe00
	v_mfma_f32_32x32x16_bf16 v[32:47], v[210:213], v[226:229], v[32:47]
	ds_read_b64_tr_b16 v[226:227], v199 offset:0x1600
	ds_read_b64_tr_b16 v[228:229], v199 offset:0x1e00
	v_mfma_f32_32x32x16_bf16 v[32:47], v[214:217], v[230:233], v[32:47]
	ds_read_b64_tr_b16 v[230:231], v199 offset:0x2600
	ds_read_b64_tr_b16 v[232:233], v199 offset:0x2e00
	v_mfma_f32_32x32x16_bf16 v[32:47], v[218:221], v[234:237], v[32:47]
	ds_read_b64_tr_b16 v[234:235], v199 offset:0x3600
	ds_read_b64_tr_b16 v[236:237], v199 offset:0x3e00
	s_waitcnt lgkmcnt(0)
	v_mfma_f32_32x32x16_bf16 v[16:31], v[206:209], v[222:225], v[16:31]
	s_andn2_b64 vcc, exec, s[6:7]
	v_mfma_f32_32x32x16_bf16 v[16:31], v[210:213], v[226:229], v[16:31]
	v_mfma_f32_32x32x16_bf16 v[16:31], v[214:217], v[230:233], v[16:31]
	v_mfma_f32_32x32x16_bf16 v[16:31], v[218:221], v[234:237], v[16:31]
	s_setprio 0
	s_cbranch_vccnz .LBB0_519
	v_max_f32_e32 v206, v65, v65
	v_max_f32_e32 v207, v64, v64
	v_max_f32_e32 v206, v207, v206
	v_max3_f32 v206, v206, v66, v67
	v_max3_f32 v206, v206, v68, v69
	v_max3_f32 v206, v206, v70, v71
	v_max3_f32 v206, v206, v72, v73
	v_max3_f32 v206, v206, v74, v75
	v_max3_f32 v206, v206, v76, v77
	v_max3_f32 v206, v206, v78, v79
	v_max3_f32 v206, v206, v80, v81
	v_max3_f32 v206, v206, v82, v83
	v_max3_f32 v206, v206, v84, v85
	v_max3_f32 v206, v206, v86, v87
	v_max3_f32 v206, v206, v88, v89
	v_max3_f32 v206, v206, v90, v91
	v_max3_f32 v206, v206, v92, v93
	v_max3_f32 v206, v206, v94, v95
	v_mov_b32_e32 v207, v206
	s_nop 1
	v_permlane32_swap_b32_e32 v206, v207
	v_max_f32_e32 v207, v207, v207
	v_max_f32_e32 v206, v206, v206
	v_max_f32_e32 v206, v206, v207
	v_sub_f32_e32 v207, v206, v195
	v_cmp_ge_f32_e32 vcc, s93, v207
	v_max_f32_e32 v207, v195, v195
	v_max_f32_e32 v207, v207, v206
	v_sub_f32_e32 v206, v195, v207
	v_mul_f32_e32 v206, 0x3dd53b94, v206
	v_exp_f32_e32 v206, v206
	s_cmp_eq_u64 vcc, exec
	s_cselect_b64 s[6:7], -1, 0
	v_cndmask_b32_e64 v206, v206, 1.0, s[6:7]
	v_cmp_gt_f32_e32 vcc, 1.0, v206
	s_cbranch_vccz .LBB0_518
	s_and_saveexec_b64 s[38:39], s[4:5]
	ds_write_b32 v197, v206 offset:128
	s_or_b64 exec, exec, s[38:39]
	s_waitcnt lgkmcnt(0)
	v_add_u32_e32 v220, s77, v196
	ds_read_b128 v[208:211], v220 offset:224
	ds_read_b128 v[212:215], v220 offset:192
	ds_read_b128 v[216:219], v220 offset:160
	ds_read_b128 v[220:223], v220 offset:128
	s_waitcnt lgkmcnt(0)
	v_pk_mul_f32 v[12:13], v[12:13], v[208:209]
	v_pk_mul_f32 v[8:9], v[8:9], v[212:213]
	v_pk_mul_f32 v[4:5], v[4:5], v[216:217]
	v_pk_mul_f32 v[14:15], v[14:15], v[210:211]
	v_pk_mul_f32 v[10:11], v[10:11], v[214:215]
	v_pk_mul_f32 v[6:7], v[6:7], v[218:219]
	v_pk_mul_f32 v[2:3], v[2:3], v[222:223]
	v_pk_mul_f32 v[0:1], v[0:1], v[220:221]
	v_pk_mul_f32 v[60:61], v[60:61], v[208:209]
	v_pk_mul_f32 v[56:57], v[56:57], v[212:213]
	v_pk_mul_f32 v[52:53], v[52:53], v[216:217]
	v_pk_mul_f32 v[62:63], v[62:63], v[210:211]
	v_pk_mul_f32 v[58:59], v[58:59], v[214:215]
	v_pk_mul_f32 v[54:55], v[54:55], v[218:219]
	v_pk_mul_f32 v[50:51], v[50:51], v[222:223]
	v_pk_mul_f32 v[48:49], v[48:49], v[220:221]
	v_pk_mul_f32 v[44:45], v[44:45], v[208:209]
	v_pk_mul_f32 v[40:41], v[40:41], v[212:213]
	v_pk_mul_f32 v[36:37], v[36:37], v[216:217]
	v_pk_mul_f32 v[46:47], v[46:47], v[210:211]
	v_pk_mul_f32 v[42:43], v[42:43], v[214:215]
	v_pk_mul_f32 v[38:39], v[38:39], v[218:219]
	v_pk_mul_f32 v[34:35], v[34:35], v[222:223]
	v_pk_mul_f32 v[32:33], v[32:33], v[220:221]
	v_pk_mul_f32 v[28:29], v[28:29], v[208:209]
	v_pk_mul_f32 v[24:25], v[24:25], v[212:213]
	v_pk_mul_f32 v[20:21], v[20:21], v[216:217]
	v_pk_mul_f32 v[30:31], v[30:31], v[210:211]
	v_pk_mul_f32 v[26:27], v[26:27], v[214:215]
	v_pk_mul_f32 v[22:23], v[22:23], v[218:219]
	v_pk_mul_f32 v[18:19], v[18:19], v[222:223]
	v_pk_mul_f32 v[16:17], v[16:17], v[220:221]

.LBB0_1407:
	v_add_f32_e32 v120, 0, v64
	v_add_f32_e32 v120, v65, v120
	v_add_f32_e32 v120, v66, v120
	ds_read_b128 v[96:99], v191 offset:40960
	ds_read_b128 v[112:115], v191 offset:45056
	ds_read_b128 v[100:103], v192 offset:40960
	ds_read_b128 v[116:119], v193 offset:40960
	ds_read_b128 v[206:209], v195 offset:40960
	ds_read_b128 v[214:217], v195 offset:45056
	ds_read_b128 v[210:213], v196 offset:40960
	ds_read_b128 v[218:221], v197 offset:40960
	v_add_f32_e32 v120, v67, v120
	s_waitcnt lgkmcnt(0)
	v_mfma_f32_32x32x64_f8f6f4 v[96:111], v[96:103], v[128:135], 0
	v_add_f32_e32 v205, v68, v120
	v_add_f32_e32 v205, v69, v205
	v_add_f32_e32 v205, v70, v205
	v_add_f32_e32 v205, v71, v205
	v_add_f32_e32 v205, v72, v205
	v_add_f32_e32 v205, v73, v205
	v_add_f32_e32 v205, v74, v205
	v_add_f32_e32 v205, v75, v205
	v_exp_f32_e32 v80, v80
	v_add_f32_e32 v205, v76, v205
	v_exp_f32_e32 v81, v81
	v_add_f32_e32 v205, v77, v205
	v_exp_f32_e32 v82, v82
	v_add_f32_e32 v205, v78, v205
	v_exp_f32_e32 v83, v83
	v_mfma_f32_32x32x64_f8f6f4 v[112:127], v[112:119], v[128:135], 0
	v_add_f32_e32 v205, v79, v205
	v_exp_f32_e32 v84, v84
	v_add_f32_e32 v205, v80, v205
	v_exp_f32_e32 v85, v85
	v_add_f32_e32 v205, v81, v205
	v_exp_f32_e32 v86, v86
	v_add_f32_e32 v205, v82, v205
	v_exp_f32_e32 v87, v87
	v_add_f32_e32 v205, v83, v205
	v_exp_f32_e32 v88, v88
	v_add_f32_e32 v205, v84, v205
	v_exp_f32_e32 v89, v89
	v_add_f32_e32 v205, v85, v205
	v_exp_f32_e32 v90, v90
	v_add_f32_e32 v205, v86, v205
	v_mfma_f32_32x32x64_f8f6f4 v[96:111], v[206:213], v[136:143], v[96:111]
	v_exp_f32_e32 v91, v91
	v_add_f32_e32 v205, v87, v205
	v_exp_f32_e32 v92, v92
	v_add_f32_e32 v205, v88, v205
	v_exp_f32_e32 v93, v93
	v_add_f32_e32 v205, v89, v205
	v_exp_f32_e32 v94, v94
	v_add_f32_e32 v205, v90, v205
	v_exp_f32_e32 v95, v95
	v_add_f32_e32 v205, v91, v205
	v_add_f32_e32 v205, v92, v205
	v_add_f32_e32 v205, v93, v205
	v_add_f32_e32 v205, v94, v205
	v_add_f32_e32 v205, v95, v205
	v_mov_b32_e32 v206, v205
	v_mfma_f32_32x32x64_f8f6f4 v[112:127], v[214:221], v[136:143], v[112:127]
	v_cvt_pk_bf16_f32 v208, v64, v65
	v_cvt_pk_bf16_f32 v209, v66, v67
	v_cvt_pk_bf16_f32 v210, v68, v69
	s_nop 0
	v_permlane32_swap_b32_e32 v205, v206
	v_cvt_pk_bf16_f32 v211, v70, v71
	v_permlane32_swap_b32_e32 v208, v210
	v_cvt_pk_bf16_f32 v212, v72, v73
	v_cvt_pk_bf16_f32 v213, v74, v75
	v_cvt_pk_bf16_f32 v214, v76, v77
	v_cvt_pk_bf16_f32 v215, v78, v79
	v_cvt_pk_bf16_f32 v216, v80, v81
	v_cvt_pk_bf16_f32 v217, v82, v83
	v_cvt_pk_bf16_f32 v218, v84, v85
	v_cvt_pk_bf16_f32 v219, v86, v87
	v_cvt_pk_bf16_f32 v220, v88, v89
	v_cvt_pk_bf16_f32 v221, v90, v91
	v_cvt_pk_bf16_f32 v222, v92, v93
	v_cvt_pk_bf16_f32 v223, v94, v95
	v_permlane32_swap_b32_e32 v209, v211
	v_permlane32_swap_b32_e32 v212, v214
	v_permlane32_swap_b32_e32 v213, v215
	v_permlane32_swap_b32_e32 v216, v218
	v_permlane32_swap_b32_e32 v217, v219
	v_permlane32_swap_b32_e32 v220, v222
	v_permlane32_swap_b32_e32 v221, v223
	ds_read_b64_tr_b16 v[224:225], v199 offset:0
	ds_read_b64_tr_b16 v[226:227], v199 offset:0x800
	ds_read_b64_tr_b16 v[228:229], v199 offset:0x1000
	ds_read_b64_tr_b16 v[230:231], v199 offset:0x1800
	ds_read_b64_tr_b16 v[232:233], v199 offset:0x2000
	ds_read_b64_tr_b16 v[234:235], v199 offset:0x2800
	ds_read_b64_tr_b16 v[236:237], v199 offset:0x3000
	ds_read_b64_tr_b16 v[238:239], v199 offset:0x3800
	s_waitcnt lgkmcnt(0)
	s_nop 0
	s_setprio 1
	v_mfma_f32_32x32x16_bf16 v[0:15], v[208:211], v[224:227], v[0:15]
	ds_read_b64_tr_b16 v[224:225], v199 offset:0x200
	ds_read_b64_tr_b16 v[226:227], v199 offset:0xa00
	v_mfma_f32_32x32x16_bf16 v[0:15], v[212:215], v[228:231], v[0:15]
	ds_read_b64_tr_b16 v[228:229], v199 offset:0x1200
	ds_read_b64_tr_b16 v[230:231], v199 offset:0x1a00
	v_mfma_f32_32x32x16_bf16 v[0:15], v[216:219], v[232:235], v[0:15]
	ds_read_b64_tr_b16 v[232:233], v199 offset:0x2200
	ds_read_b64_tr_b16 v[234:235], v199 offset:0x2a00
	ds_read_b64_tr_b16 v[240:241], v199 offset:0x3200
	ds_read_b64_tr_b16 v[242:243], v199 offset:0x3a00
	s_waitcnt lgkmcnt(0)
	v_mfma_f32_32x32x16_bf16 v[0:15], v[220:223], v[236:239], v[0:15]
	v_mfma_f32_32x32x16_bf16 v[48:63], v[208:211], v[224:227], v[48:63]
	ds_read_b64_tr_b16 v[224:225], v199 offset:0x400
	ds_read_b64_tr_b16 v[226:227], v199 offset:0xc00
	v_mfma_f32_32x32x16_bf16 v[48:63], v[212:215], v[228:231], v[48:63]
	ds_read_b64_tr_b16 v[228:229], v199 offset:0x1400
	ds_read_b64_tr_b16 v[230:231], v199 offset:0x1c00
	v_mfma_f32_32x32x16_bf16 v[48:63], v[216:219], v[232:235], v[48:63]
	ds_read_b64_tr_b16 v[232:233], v199 offset:0x2400
	ds_read_b64_tr_b16 v[234:235], v199 offset:0x2c00
	ds_read_b64_tr_b16 v[236:237], v199 offset:0x3400
	ds_read_b64_tr_b16 v[238:239], v199 offset:0x3c00
	s_waitcnt lgkmcnt(0)
	v_mfma_f32_32x32x16_bf16 v[48:63], v[220:223], v[240:243], v[48:63]
	v_mfma_f32_32x32x16_bf16 v[32:47], v[208:211], v[224:227], v[32:47]
	ds_read_b64_tr_b16 v[224:225], v199 offset:0x600
	ds_read_b64_tr_b16 v[226:227], v199 offset:0xe00
	v_mfma_f32_32x32x16_bf16 v[32:47], v[212:215], v[228:231], v[32:47]
	ds_read_b64_tr_b16 v[228:229], v199 offset:0x1600
	ds_read_b64_tr_b16 v[230:231], v199 offset:0x1e00
	v_mfma_f32_32x32x16_bf16 v[32:47], v[216:219], v[232:235], v[32:47]
	ds_read_b64_tr_b16 v[232:233], v199 offset:0x2600
	ds_read_b64_tr_b16 v[234:235], v199 offset:0x2e00
	ds_read_b64_tr_b16 v[240:241], v199 offset:0x3600
	ds_read_b64_tr_b16 v[242:243], v199 offset:0x3e00
	s_waitcnt lgkmcnt(0)
	v_mfma_f32_32x32x16_bf16 v[32:47], v[220:223], v[236:239], v[32:47]
	v_mfma_f32_32x32x16_bf16 v[16:31], v[208:211], v[224:227], v[16:31]
	v_max_f32_e32 v207, v97, v97
	v_max_f32_e32 v236, v96, v96
	v_max_f32_e32 v207, v236, v207
	v_max3_f32 v207, v207, v98, v99
	v_max3_f32 v207, v207, v100, v101
	v_max3_f32 v207, v207, v102, v103
	v_max3_f32 v207, v207, v104, v105
	v_max3_f32 v207, v207, v106, v107
	v_mfma_f32_32x32x16_bf16 v[16:31], v[212:215], v[228:231], v[16:31]
	v_max3_f32 v207, v207, v108, v109
	v_max3_f32 v207, v207, v110, v111
	v_max3_f32 v207, v207, v112, v113
	v_max3_f32 v207, v207, v114, v115
	v_max3_f32 v207, v207, v116, v117
	v_max3_f32 v207, v207, v118, v119
	v_max3_f32 v207, v207, v120, v121
	v_max3_f32 v207, v207, v122, v123
	v_mfma_f32_32x32x16_bf16 v[16:31], v[216:219], v[232:235], v[16:31]
	v_max3_f32 v207, v207, v124, v125
	v_max3_f32 v207, v207, v126, v127
	v_mov_b32_e32 v208, v207
	s_nop 1
	v_permlane32_swap_b32_e32 v207, v208
	v_max_f32_e32 v208, v208, v208
	v_max_f32_e32 v207, v207, v207
	v_max_f32_e32 v207, v207, v208
	v_max_f32_e32 v208, v198, v198
	v_max_f32_e32 v208, v208, v207
	v_sub_f32_e32 v209, v207, v198
	v_mfma_f32_32x32x16_bf16 v[16:31], v[220:223], v[240:243], v[16:31]
	s_setprio 0
	v_sub_f32_e32 v207, v198, v208
	v_mul_f32_e32 v207, 0x3e0293ee, v207
	v_exp_f32_e32 v207, v207
	v_cmp_ge_f32_e32 vcc, s22, v209
	s_cmp_eq_u64 vcc, exec
	s_cselect_b64 s[6:7], -1, 0
	v_cndmask_b32_e64 v207, v207, 1.0, s[6:7]
	v_cmp_gt_f32_e32 vcc, 1.0, v207
	s_cbranch_vccz .LBB0_1411
	s_and_saveexec_b64 s[38:39], s[4:5]
	ds_write_b32 v202, v207 offset:49280
	s_or_b64 exec, exec, s[38:39]
	s_waitcnt lgkmcnt(0)
	v_add_u32_e32 v209, s81, v201
	ds_read_b128 v[210:213], v209 offset:49376
	ds_read_b128 v[214:217], v209 offset:49344
	ds_read_b128 v[218:221], v209 offset:49312
	ds_read_b128 v[222:225], v209 offset:49280
	s_waitcnt lgkmcnt(0)
	v_pk_mul_f32 v[12:13], v[12:13], v[210:211]
	v_pk_mul_f32 v[8:9], v[8:9], v[214:215]
	v_pk_mul_f32 v[4:5], v[4:5], v[218:219]
	v_pk_mul_f32 v[14:15], v[14:15], v[212:213]
	v_pk_mul_f32 v[10:11], v[10:11], v[216:217]
	v_pk_mul_f32 v[6:7], v[6:7], v[220:221]
	v_pk_mul_f32 v[2:3], v[2:3], v[224:225]
	v_pk_mul_f32 v[0:1], v[0:1], v[222:223]
	v_pk_mul_f32 v[60:61], v[60:61], v[210:211]
	v_pk_mul_f32 v[56:57], v[56:57], v[214:215]
	v_pk_mul_f32 v[52:53], v[52:53], v[218:219]
	v_pk_mul_f32 v[62:63], v[62:63], v[212:213]
	v_pk_mul_f32 v[58:59], v[58:59], v[216:217]
	v_pk_mul_f32 v[54:55], v[54:55], v[220:221]
	v_pk_mul_f32 v[50:51], v[50:51], v[224:225]
	v_pk_mul_f32 v[48:49], v[48:49], v[222:223]
	v_pk_mul_f32 v[44:45], v[44:45], v[210:211]
	v_pk_mul_f32 v[40:41], v[40:41], v[214:215]
	v_pk_mul_f32 v[36:37], v[36:37], v[218:219]
	v_pk_mul_f32 v[46:47], v[46:47], v[212:213]
	v_pk_mul_f32 v[42:43], v[42:43], v[216:217]
	v_pk_mul_f32 v[38:39], v[38:39], v[220:221]
	v_pk_mul_f32 v[34:35], v[34:35], v[224:225]
	v_pk_mul_f32 v[32:33], v[32:33], v[222:223]
	v_pk_mul_f32 v[28:29], v[28:29], v[210:211]
	v_pk_mul_f32 v[24:25], v[24:25], v[214:215]
	v_pk_mul_f32 v[20:21], v[20:21], v[218:219]
	v_pk_mul_f32 v[30:31], v[30:31], v[212:213]
	v_pk_mul_f32 v[26:27], v[26:27], v[216:217]
	v_pk_mul_f32 v[22:23], v[22:23], v[220:221]
	v_pk_mul_f32 v[18:19], v[18:19], v[224:225]
	v_pk_mul_f32 v[16:17], v[16:17], v[222:223]

.LBB0_1413:
	v_cndmask_b32_e64 v198, v208, v198, s[6:7]
	v_mul_f32_e32 v208, 0xbe0293ee, v198
	v_fmamk_f32 v96, v96, 0x3e0293ee, v208
	v_fmamk_f32 v97, v97, 0x3e0293ee, v208
	v_fmamk_f32 v98, v98, 0x3e0293ee, v208
	v_fmamk_f32 v99, v99, 0x3e0293ee, v208
	v_fmamk_f32 v100, v100, 0x3e0293ee, v208
	v_fmamk_f32 v101, v101, 0x3e0293ee, v208
	v_fmamk_f32 v102, v102, 0x3e0293ee, v208
	v_fmamk_f32 v103, v103, 0x3e0293ee, v208
	v_fmamk_f32 v104, v104, 0x3e0293ee, v208
	v_fmamk_f32 v105, v105, 0x3e0293ee, v208
	v_fmamk_f32 v106, v106, 0x3e0293ee, v208
	v_fmamk_f32 v107, v107, 0x3e0293ee, v208
	v_fmamk_f32 v108, v108, 0x3e0293ee, v208
	v_fmamk_f32 v109, v109, 0x3e0293ee, v208
	v_fmamk_f32 v110, v110, 0x3e0293ee, v208
	v_fmamk_f32 v111, v111, 0x3e0293ee, v208
	v_fmamk_f32 v112, v112, 0x3e0293ee, v208
	v_fmamk_f32 v113, v113, 0x3e0293ee, v208
	v_fmamk_f32 v114, v114, 0x3e0293ee, v208
	v_fmamk_f32 v115, v115, 0x3e0293ee, v208
	v_fmamk_f32 v116, v116, 0x3e0293ee, v208
	v_fmamk_f32 v117, v117, 0x3e0293ee, v208
	v_fmamk_f32 v118, v118, 0x3e0293ee, v208
	v_fmamk_f32 v119, v119, 0x3e0293ee, v208
	v_fmamk_f32 v120, v120, 0x3e0293ee, v208
	v_fmamk_f32 v121, v121, 0x3e0293ee, v208
	v_fmamk_f32 v122, v122, 0x3e0293ee, v208
	v_fmamk_f32 v123, v123, 0x3e0293ee, v208
	v_fmamk_f32 v124, v124, 0x3e0293ee, v208
	v_fmamk_f32 v125, v125, 0x3e0293ee, v208
	v_fmamk_f32 v126, v126, 0x3e0293ee, v208
	v_fmac_f32_e32 v208, 0x3e0293ee, v127
	v_exp_f32_e32 v127, v96
	v_exp_f32_e32 v209, v97
	v_exp_f32_e32 v210, v98
	v_exp_f32_e32 v99, v99
	v_exp_f32_e32 v100, v100
	v_add_f32_e32 v96, 0, v127
	v_exp_f32_e32 v101, v101
	v_add_f32_e32 v96, v209, v96
	v_exp_f32_e32 v102, v102
	v_add_f32_e32 v96, v210, v96
	v_exp_f32_e32 v103, v103
	v_add_f32_e32 v96, v99, v96
	v_exp_f32_e32 v104, v104
	v_add_f32_e32 v96, v100, v96
	v_exp_f32_e32 v105, v105
	v_add_f32_e32 v96, v101, v96
	v_exp_f32_e32 v106, v106
	v_add_f32_e32 v96, v102, v96
	v_exp_f32_e32 v107, v107
	v_add_f32_e32 v96, v103, v96
	v_exp_f32_e32 v108, v108
	v_add_f32_e32 v96, v104, v96
	v_exp_f32_e32 v109, v109
	v_add_f32_e32 v96, v105, v96
	v_exp_f32_e32 v110, v110
	v_add_f32_e32 v96, v106, v96
	v_exp_f32_e32 v111, v111
	v_add_f32_e32 v96, v107, v96
	v_exp_f32_e32 v112, v112
	v_add_f32_e32 v96, v108, v96
	v_exp_f32_e32 v113, v113
	v_add_f32_e32 v96, v109, v96
	v_exp_f32_e32 v114, v114
	v_add_f32_e32 v96, v110, v96
	v_exp_f32_e32 v115, v115
	v_add_f32_e32 v96, v111, v96
	v_exp_f32_e32 v116, v116
	v_add_f32_e32 v96, v112, v96
	v_exp_f32_e32 v117, v117
	v_add_f32_e32 v96, v113, v96
	v_exp_f32_e32 v118, v118
	v_add_f32_e32 v96, v114, v96
	v_exp_f32_e32 v119, v119
	v_add_f32_e32 v96, v115, v96
	v_exp_f32_e32 v120, v120
	v_add_f32_e32 v96, v116, v96
	v_exp_f32_e32 v121, v121
	v_add_f32_e32 v96, v117, v96
	v_exp_f32_e32 v122, v122
	v_add_f32_e32 v96, v118, v96
	v_exp_f32_e32 v123, v123
	v_add_f32_e32 v96, v119, v96
	v_exp_f32_e32 v124, v124
	v_add_f32_e32 v96, v120, v96
	v_exp_f32_e32 v125, v125
	v_add_f32_e32 v96, v121, v96
	v_exp_f32_e32 v126, v126
	v_add_f32_e32 v96, v122, v96
	v_exp_f32_e32 v208, v208
	v_add_f32_e32 v96, v123, v96
	v_add_f32_e32 v96, v124, v96
	v_add_f32_e32 v96, v125, v96
	v_add_f32_e32 v96, v126, v96
	v_add_f32_e32 v96, v208, v96
	v_mov_b32_e32 v97, v96
	s_nop 1
	v_permlane32_swap_b32_e32 v96, v97
	v_cvt_pk_bf16_f32 v98, v127, v209
	v_cvt_pk_bf16_f32 v99, v210, v99
	v_cvt_pk_bf16_f32 v100, v100, v101
	v_cvt_pk_bf16_f32 v101, v102, v103
	v_cvt_pk_bf16_f32 v102, v104, v105
	v_cvt_pk_bf16_f32 v103, v106, v107
	v_cvt_pk_bf16_f32 v104, v108, v109
	v_cvt_pk_bf16_f32 v105, v110, v111
	v_cvt_pk_bf16_f32 v106, v112, v113
	v_cvt_pk_bf16_f32 v107, v114, v115
	v_cvt_pk_bf16_f32 v108, v116, v117
	v_cvt_pk_bf16_f32 v109, v118, v119
	v_cvt_pk_bf16_f32 v110, v120, v121
	v_cvt_pk_bf16_f32 v111, v122, v123
	v_cvt_pk_bf16_f32 v112, v124, v125
	v_cvt_pk_bf16_f32 v113, v126, v208
	s_nop 0
	v_permlane32_swap_b32_e32 v98, v100
	v_permlane32_swap_b32_e32 v99, v101
	v_permlane32_swap_b32_e32 v102, v104
	v_permlane32_swap_b32_e32 v103, v105
	v_permlane32_swap_b32_e32 v106, v108
	v_permlane32_swap_b32_e32 v107, v109
	v_permlane32_swap_b32_e32 v110, v112
	v_permlane32_swap_b32_e32 v111, v113
	ds_read_b64_tr_b16 v[114:115], v204 offset:0
	ds_read_b64_tr_b16 v[116:117], v204 offset:0x800
	ds_read_b64_tr_b16 v[118:119], v204 offset:0x1000
	ds_read_b64_tr_b16 v[120:121], v204 offset:0x1800
	ds_read_b64_tr_b16 v[122:123], v204 offset:0x2000
	ds_read_b64_tr_b16 v[124:125], v204 offset:0x2800
	ds_read_b64_tr_b16 v[208:209], v204 offset:0x3000
	ds_read_b64_tr_b16 v[210:211], v204 offset:0x3800
	s_waitcnt lgkmcnt(0)
	s_nop 0
	s_setprio 1
	v_mfma_f32_32x32x16_bf16 v[0:15], v[98:101], v[114:117], v[0:15]
	ds_read_b64_tr_b16 v[114:115], v204 offset:0x200
	ds_read_b64_tr_b16 v[116:117], v204 offset:0xa00
	v_mfma_f32_32x32x16_bf16 v[0:15], v[102:105], v[118:121], v[0:15]
	ds_read_b64_tr_b16 v[118:119], v204 offset:0x1200
	ds_read_b64_tr_b16 v[120:121], v204 offset:0x1a00
	v_mfma_f32_32x32x16_bf16 v[0:15], v[106:109], v[122:125], v[0:15]
	ds_read_b64_tr_b16 v[122:123], v204 offset:0x2200
	ds_read_b64_tr_b16 v[124:125], v204 offset:0x2a00
	ds_read_b64_tr_b16 v[212:213], v204 offset:0x3200
	ds_read_b64_tr_b16 v[214:215], v204 offset:0x3a00
	s_waitcnt lgkmcnt(0)
	v_mfma_f32_32x32x16_bf16 v[0:15], v[110:113], v[208:211], v[0:15]
	v_mfma_f32_32x32x16_bf16 v[48:63], v[98:101], v[114:117], v[48:63]
	ds_read_b64_tr_b16 v[114:115], v204 offset:0x400
	ds_read_b64_tr_b16 v[116:117], v204 offset:0xc00
	v_mfma_f32_32x32x16_bf16 v[48:63], v[102:105], v[118:121], v[48:63]
	ds_read_b64_tr_b16 v[118:119], v204 offset:0x1400
	ds_read_b64_tr_b16 v[120:121], v204 offset:0x1c00
	v_mfma_f32_32x32x16_bf16 v[48:63], v[106:109], v[122:125], v[48:63]
	ds_read_b64_tr_b16 v[122:123], v204 offset:0x2400
	ds_read_b64_tr_b16 v[124:125], v204 offset:0x2c00
	ds_read_b64_tr_b16 v[208:209], v204 offset:0x3400
	ds_read_b64_tr_b16 v[210:211], v204 offset:0x3c00
	s_waitcnt lgkmcnt(0)
	v_mfma_f32_32x32x16_bf16 v[48:63], v[110:113], v[212:215], v[48:63]
	v_mfma_f32_32x32x16_bf16 v[32:47], v[98:101], v[114:117], v[32:47]
	ds_read_b64_tr_b16 v[114:115], v204 offset:0x600
	ds_read_b64_tr_b16 v[116:117], v204 offset:0xe00
	v_mfma_f32_32x32x16_bf16 v[32:47], v[102:105], v[118:121], v[32:47]
	ds_read_b64_tr_b16 v[118:119], v204 offset:0x1600
	ds_read_b64_tr_b16 v[120:121], v204 offset:0x1e00
	v_mfma_f32_32x32x16_bf16 v[32:47], v[106:109], v[122:125], v[32:47]
	ds_read_b64_tr_b16 v[122:123], v204 offset:0x2600
	ds_read_b64_tr_b16 v[124:125], v204 offset:0x2e00
	ds_read_b64_tr_b16 v[212:213], v204 offset:0x3600
	ds_read_b64_tr_b16 v[214:215], v204 offset:0x3e00
	s_waitcnt lgkmcnt(0)
	v_mfma_f32_32x32x16_bf16 v[32:47], v[110:113], v[208:211], v[32:47]
	v_mfma_f32_32x32x16_bf16 v[16:31], v[98:101], v[114:117], v[16:31]
	s_andn2_b64 vcc, exec, s[40:41]
	v_mfma_f32_32x32x16_bf16 v[16:31], v[102:105], v[118:121], v[16:31]
	v_mfma_f32_32x32x16_bf16 v[16:31], v[106:109], v[122:125], v[16:31]
	v_mfma_f32_32x32x16_bf16 v[16:31], v[110:113], v[212:215], v[16:31]
	s_setprio 0
	s_cbranch_vccnz .LBB0_1419
	v_max_f32_e32 v98, v65, v65
	v_max_f32_e32 v99, v64, v64
	v_max_f32_e32 v98, v99, v98
	v_max3_f32 v98, v98, v66, v67
	v_max3_f32 v98, v98, v68, v69
	v_max3_f32 v98, v98, v70, v71
	v_max3_f32 v98, v98, v72, v73
	v_max3_f32 v98, v98, v74, v75
	v_max3_f32 v98, v98, v76, v77
	v_max3_f32 v98, v98, v78, v79
	v_max3_f32 v98, v98, v80, v81
	v_max3_f32 v98, v98, v82, v83
	v_max3_f32 v98, v98, v84, v85
	v_max3_f32 v98, v98, v86, v87
	v_max3_f32 v98, v98, v88, v89
	v_max3_f32 v98, v98, v90, v91
	v_max3_f32 v98, v98, v92, v93
	v_max3_f32 v98, v98, v94, v95
	v_mov_b32_e32 v99, v98
	s_nop 1
	v_permlane32_swap_b32_e32 v98, v99
	v_max_f32_e32 v99, v99, v99
	v_max_f32_e32 v98, v98, v98
	v_max_f32_e32 v98, v98, v99
	v_sub_f32_e32 v99, v98, v198
	v_cmp_ge_f32_e32 vcc, s22, v99
	v_max_f32_e32 v99, v198, v198
	v_max_f32_e32 v99, v99, v98
	v_sub_f32_e32 v98, v198, v99
	v_mul_f32_e32 v98, 0x3e0293ee, v98
	v_exp_f32_e32 v98, v98
	s_cmp_eq_u64 vcc, exec
	s_cselect_b64 s[6:7], -1, 0
	v_cndmask_b32_e64 v98, v98, 1.0, s[6:7]
	v_cmp_gt_f32_e32 vcc, 1.0, v98
	s_cbranch_vccz .LBB0_1418
	s_and_saveexec_b64 s[40:41], s[4:5]
	ds_write_b32 v202, v98 offset:49280
	s_or_b64 exec, exec, s[40:41]
	s_waitcnt lgkmcnt(0)
	v_add_u32_e32 v112, s81, v201
	ds_read_b128 v[100:103], v112 offset:49376
	ds_read_b128 v[104:107], v112 offset:49344
	ds_read_b128 v[108:111], v112 offset:49312
	ds_read_b128 v[112:115], v112 offset:49280
	s_waitcnt lgkmcnt(0)
	v_pk_mul_f32 v[12:13], v[12:13], v[100:101]
	v_pk_mul_f32 v[8:9], v[8:9], v[104:105]
	v_pk_mul_f32 v[4:5], v[4:5], v[108:109]
	v_pk_mul_f32 v[14:15], v[14:15], v[102:103]
	v_pk_mul_f32 v[10:11], v[10:11], v[106:107]
	v_pk_mul_f32 v[6:7], v[6:7], v[110:111]
	v_pk_mul_f32 v[2:3], v[2:3], v[114:115]
	v_pk_mul_f32 v[0:1], v[0:1], v[112:113]
	v_pk_mul_f32 v[60:61], v[60:61], v[100:101]
	v_pk_mul_f32 v[56:57], v[56:57], v[104:105]
	v_pk_mul_f32 v[52:53], v[52:53], v[108:109]
	v_pk_mul_f32 v[62:63], v[62:63], v[102:103]
	v_pk_mul_f32 v[58:59], v[58:59], v[106:107]
	v_pk_mul_f32 v[54:55], v[54:55], v[110:111]
	v_pk_mul_f32 v[50:51], v[50:51], v[114:115]
	v_pk_mul_f32 v[48:49], v[48:49], v[112:113]
	v_pk_mul_f32 v[44:45], v[44:45], v[100:101]
	v_pk_mul_f32 v[40:41], v[40:41], v[104:105]
	v_pk_mul_f32 v[36:37], v[36:37], v[108:109]
	v_pk_mul_f32 v[46:47], v[46:47], v[102:103]
	v_pk_mul_f32 v[42:43], v[42:43], v[106:107]
	v_pk_mul_f32 v[38:39], v[38:39], v[110:111]
	v_pk_mul_f32 v[34:35], v[34:35], v[114:115]
	v_pk_mul_f32 v[32:33], v[32:33], v[112:113]
	v_pk_mul_f32 v[28:29], v[28:29], v[100:101]
	v_pk_mul_f32 v[24:25], v[24:25], v[104:105]
	v_pk_mul_f32 v[20:21], v[20:21], v[108:109]
	v_pk_mul_f32 v[30:31], v[30:31], v[102:103]
	v_pk_mul_f32 v[26:27], v[26:27], v[106:107]
	v_pk_mul_f32 v[22:23], v[22:23], v[110:111]
	v_pk_mul_f32 v[18:19], v[18:19], v[114:115]
	v_pk_mul_f32 v[16:17], v[16:17], v[112:113]
